# accumulator zeroing between GEMM units with v_pk_mov_b32 register pairs instead of one v_mov_b32 per register
# speedup vs baseline: 1.0146x; 1.0075x over previous
.LBB0_197:
	s_and_b64 s[6:7], s[30:31], exec
	s_cselect_b32 s5, s25, s35
	s_cselect_b32 s11, s24, s34
	s_cselect_b32 s21, s27, s63
	s_cselect_b32 s23, s26, s62
	s_cselect_b32 vcc_lo, s29, s37
	s_cselect_b32 vcc_hi, s28, s36
	s_add_u32 s8, s62, 0x100
	s_addc_u32 s6, s63, 0
	s_add_u32 s7, s36, 0x100
	v_mov_b32_e32 v32, 0
	s_addc_u32 s33, s37, 0
	s_mov_b32 s9, -2
	v_mov_b32_e32 v33, v32
	v_pk_mov_b32 v[34:35], v[32:33], v[32:33]
	v_pk_mov_b32 v[36:37], v[32:33], v[32:33]
	v_pk_mov_b32 v[38:39], v[32:33], v[32:33]
	v_pk_mov_b32 v[48:49], v[32:33], v[32:33]
	v_pk_mov_b32 v[50:51], v[32:33], v[32:33]
	v_pk_mov_b32 v[52:53], v[32:33], v[32:33]
	v_pk_mov_b32 v[54:55], v[32:33], v[32:33]
	v_pk_mov_b32 v[0:1], v[32:33], v[32:33]
	v_pk_mov_b32 v[2:3], v[32:33], v[32:33]
	v_pk_mov_b32 v[12:13], v[32:33], v[32:33]
	v_pk_mov_b32 v[14:15], v[32:33], v[32:33]
	v_pk_mov_b32 v[24:25], v[32:33], v[32:33]
	v_pk_mov_b32 v[26:27], v[32:33], v[32:33]
	v_pk_mov_b32 v[28:29], v[32:33], v[32:33]
	v_pk_mov_b32 v[30:31], v[32:33], v[32:33]
	v_pk_mov_b32 v[40:41], v[32:33], v[32:33]
	v_pk_mov_b32 v[42:43], v[32:33], v[32:33]
	v_pk_mov_b32 v[44:45], v[32:33], v[32:33]
	v_pk_mov_b32 v[46:47], v[32:33], v[32:33]
	v_pk_mov_b32 v[56:57], v[32:33], v[32:33]
	v_pk_mov_b32 v[58:59], v[32:33], v[32:33]
	v_pk_mov_b32 v[60:61], v[32:33], v[32:33]
	v_pk_mov_b32 v[62:63], v[32:33], v[32:33]
	v_pk_mov_b32 v[64:65], v[32:33], v[32:33]
	v_pk_mov_b32 v[66:67], v[32:33], v[32:33]
	v_pk_mov_b32 v[68:69], v[32:33], v[32:33]
	v_pk_mov_b32 v[70:71], v[32:33], v[32:33]
	v_pk_mov_b32 v[80:81], v[32:33], v[32:33]
	v_pk_mov_b32 v[82:83], v[32:33], v[32:33]
	v_pk_mov_b32 v[84:85], v[32:33], v[32:33]
	v_pk_mov_b32 v[86:87], v[32:33], v[32:33]
	v_pk_mov_b32 v[96:97], v[32:33], v[32:33]
	v_pk_mov_b32 v[98:99], v[32:33], v[32:33]
	v_pk_mov_b32 v[100:101], v[32:33], v[32:33]
	v_pk_mov_b32 v[102:103], v[32:33], v[32:33]
	v_pk_mov_b32 v[112:113], v[32:33], v[32:33]
	v_pk_mov_b32 v[114:115], v[32:33], v[32:33]
	v_pk_mov_b32 v[116:117], v[32:33], v[32:33]
	v_pk_mov_b32 v[118:119], v[32:33], v[32:33]
	v_pk_mov_b32 v[72:73], v[32:33], v[32:33]
	v_pk_mov_b32 v[74:75], v[32:33], v[32:33]
	v_pk_mov_b32 v[76:77], v[32:33], v[32:33]
	v_pk_mov_b32 v[78:79], v[32:33], v[32:33]
	v_pk_mov_b32 v[88:89], v[32:33], v[32:33]
	v_pk_mov_b32 v[90:91], v[32:33], v[32:33]
	v_pk_mov_b32 v[92:93], v[32:33], v[32:33]
	v_pk_mov_b32 v[94:95], v[32:33], v[32:33]
	v_pk_mov_b32 v[104:105], v[32:33], v[32:33]
	v_pk_mov_b32 v[106:107], v[32:33], v[32:33]
	v_pk_mov_b32 v[108:109], v[32:33], v[32:33]
	v_pk_mov_b32 v[110:111], v[32:33], v[32:33]
	v_pk_mov_b32 v[120:121], v[32:33], v[32:33]
	v_pk_mov_b32 v[122:123], v[32:33], v[32:33]
	v_pk_mov_b32 v[124:125], v[32:33], v[32:33]
	v_pk_mov_b32 v[126:127], v[32:33], v[32:33]
	v_pk_mov_b32 v[20:21], v[32:33], v[32:33]
	v_pk_mov_b32 v[22:23], v[32:33], v[32:33]
	v_pk_mov_b32 v[16:17], v[32:33], v[32:33]
	v_pk_mov_b32 v[18:19], v[32:33], v[32:33]
	v_pk_mov_b32 v[8:9], v[32:33], v[32:33]
	v_pk_mov_b32 v[10:11], v[32:33], v[32:33]
	v_pk_mov_b32 v[4:5], v[32:33], v[32:33]
	v_pk_mov_b32 v[6:7], v[32:33], v[32:33]

.LBB0_517:
	s_and_b64 s[40:41], s[28:29], exec
	s_cselect_b32 s19, s23, s31
	s_cselect_b32 s21, s22, s30
	s_cselect_b32 s40, s25, s37
	s_cselect_b32 s41, s24, s36
	s_cselect_b32 s42, s27, s57
	s_cselect_b32 s43, s26, s56
	s_lshl_b32 s33, s34, 8
	s_lshl_b32 s34, s35, 8
	s_add_i32 s33, s33, s4
	s_or_b32 s82, s34, s5
	s_add_u32 s44, s36, 0x100
	s_addc_u32 s45, s37, 0
	s_add_u32 s46, s56, 0x100
	v_mov_b32_e32 v32, 0
	s_addc_u32 s47, s57, 0
	s_mov_b32 s48, -2
	v_mov_b32_e32 v33, v32
	v_pk_mov_b32 v[34:35], v[32:33], v[32:33]
	v_pk_mov_b32 v[36:37], v[32:33], v[32:33]
	v_pk_mov_b32 v[38:39], v[32:33], v[32:33]
	v_pk_mov_b32 v[48:49], v[32:33], v[32:33]
	v_pk_mov_b32 v[50:51], v[32:33], v[32:33]
	v_pk_mov_b32 v[52:53], v[32:33], v[32:33]
	v_pk_mov_b32 v[54:55], v[32:33], v[32:33]
	v_pk_mov_b32 v[0:1], v[32:33], v[32:33]
	v_pk_mov_b32 v[2:3], v[32:33], v[32:33]
	v_pk_mov_b32 v[4:5], v[32:33], v[32:33]
	v_pk_mov_b32 v[6:7], v[32:33], v[32:33]
	v_pk_mov_b32 v[16:17], v[32:33], v[32:33]
	v_pk_mov_b32 v[18:19], v[32:33], v[32:33]
	v_pk_mov_b32 v[20:21], v[32:33], v[32:33]
	v_pk_mov_b32 v[22:23], v[32:33], v[32:33]
	v_pk_mov_b32 v[40:41], v[32:33], v[32:33]
	v_pk_mov_b32 v[42:43], v[32:33], v[32:33]
	s_waitcnt vmcnt(4)
	v_pk_mov_b32 v[44:45], v[32:33], v[32:33]
	v_pk_mov_b32 v[46:47], v[32:33], v[32:33]
	v_pk_mov_b32 v[56:57], v[32:33], v[32:33]
	v_pk_mov_b32 v[58:59], v[32:33], v[32:33]
	v_pk_mov_b32 v[60:61], v[32:33], v[32:33]
	v_pk_mov_b32 v[62:63], v[32:33], v[32:33]
	v_pk_mov_b32 v[64:65], v[32:33], v[32:33]
	v_pk_mov_b32 v[66:67], v[32:33], v[32:33]
	v_pk_mov_b32 v[68:69], v[32:33], v[32:33]
	v_pk_mov_b32 v[70:71], v[32:33], v[32:33]
	v_pk_mov_b32 v[80:81], v[32:33], v[32:33]
	v_pk_mov_b32 v[82:83], v[32:33], v[32:33]
	v_pk_mov_b32 v[84:85], v[32:33], v[32:33]
	v_pk_mov_b32 v[86:87], v[32:33], v[32:33]
	v_pk_mov_b32 v[96:97], v[32:33], v[32:33]
	v_pk_mov_b32 v[98:99], v[32:33], v[32:33]
	v_pk_mov_b32 v[100:101], v[32:33], v[32:33]
	v_pk_mov_b32 v[102:103], v[32:33], v[32:33]
	v_pk_mov_b32 v[112:113], v[32:33], v[32:33]
	v_pk_mov_b32 v[114:115], v[32:33], v[32:33]
	v_pk_mov_b32 v[116:117], v[32:33], v[32:33]
	v_pk_mov_b32 v[118:119], v[32:33], v[32:33]
	v_pk_mov_b32 v[72:73], v[32:33], v[32:33]
	v_pk_mov_b32 v[74:75], v[32:33], v[32:33]
	v_pk_mov_b32 v[76:77], v[32:33], v[32:33]
	v_pk_mov_b32 v[78:79], v[32:33], v[32:33]
	v_pk_mov_b32 v[88:89], v[32:33], v[32:33]
	v_pk_mov_b32 v[90:91], v[32:33], v[32:33]
	v_pk_mov_b32 v[92:93], v[32:33], v[32:33]
	v_pk_mov_b32 v[94:95], v[32:33], v[32:33]
	v_pk_mov_b32 v[104:105], v[32:33], v[32:33]
	v_pk_mov_b32 v[106:107], v[32:33], v[32:33]
	v_pk_mov_b32 v[108:109], v[32:33], v[32:33]
	v_pk_mov_b32 v[110:111], v[32:33], v[32:33]
	v_pk_mov_b32 v[120:121], v[32:33], v[32:33]
	v_pk_mov_b32 v[122:123], v[32:33], v[32:33]
	v_pk_mov_b32 v[124:125], v[32:33], v[32:33]
	v_pk_mov_b32 v[126:127], v[32:33], v[32:33]
	v_pk_mov_b32 v[28:29], v[32:33], v[32:33]
	v_pk_mov_b32 v[30:31], v[32:33], v[32:33]
	v_pk_mov_b32 v[24:25], v[32:33], v[32:33]
	v_pk_mov_b32 v[26:27], v[32:33], v[32:33]
	v_pk_mov_b32 v[12:13], v[32:33], v[32:33]
	v_pk_mov_b32 v[14:15], v[32:33], v[32:33]
	v_pk_mov_b32 v[8:9], v[32:33], v[32:33]
	v_pk_mov_b32 v[10:11], v[32:33], v[32:33]
	s_branch .LBB0_519

.LBB0_683:
	v_readlane_b32 s11, v255, 0
	s_bfe_u32 s2, s11, 0x20006
	s_lshl_b32 s0, s1, 6
	v_and_b32_e32 v2, 48, v0
	v_lshlrev_b32_e32 v4, 6, v0
	s_movk_i32 s10, 0x3c0
	s_add_u32 s20, s14, 0x80
	v_and_or_b32 v2, v4, s10, v2
	s_waitcnt vmcnt(2)
	s_barrier
	s_addc_u32 s21, s15, 0
	s_add_i32 s49, s5, 0x18000
	s_mov_b32 s10, m0
	s_mov_b32 m0, s49
	s_nop 2
	global_load_lds_dwordx4 v137, s[20:21]
	s_mov_b32 m0, s10
	s_add_i32 s50, s5, 0x1a000
	s_mov_b32 s10, m0
	s_mov_b32 m0, s50
	s_nop 2
	global_load_lds_dwordx4 v254, s[20:21]
	s_mov_b32 m0, s10
	s_add_u32 s20, s6, 0x80
	s_addc_u32 s21, s7, 0
	s_add_i32 s51, s5, 0x8000
	s_mov_b32 s10, m0
	s_mov_b32 m0, s51
	s_nop 2
	global_load_lds_dwordx4 v132, s[20:21]
	s_mov_b32 m0, s10
	s_add_i32 s52, s5, 0xa000
	s_mov_b32 s10, m0
	s_mov_b32 m0, s52
	s_nop 2
	global_load_lds_dwordx4 v133, s[20:21]
	s_mov_b32 m0, s10
	s_add_u32 s20, s14, 0x40080
	s_addc_u32 s21, s15, 0
	s_add_i32 s53, s5, 0x1c000
	s_mov_b32 s10, m0
	s_mov_b32 m0, s53
	s_nop 2
	global_load_lds_dwordx4 v137, s[20:21]
	s_mov_b32 m0, s10
	v_and_b32_e32 v1, 0xfffffc00, v1
	v_lshlrev_b32_e32 v0, 2, v0
	s_add_i32 s54, s5, 0x1e000
	s_mov_b32 s10, m0
	s_mov_b32 m0, s54
	s_nop 2
	global_load_lds_dwordx4 v254, s[20:21]
	s_mov_b32 m0, s10
	v_lshl_add_u32 v3, s1, 13, v1
	v_and_b32_e32 v0, 32, v0
	v_lshl_add_u32 v1, s2, 12, v1
	s_waitcnt vmcnt(6)
	s_add_i32 s55, s5, 0xc000
	v_bitop3_b32 v3, v2, v3, v0 bitop3:0xde
	v_bitop3_b32 v0, v2, v1, v0 bitop3:0xde
	s_cmpk_lt_u32 s11, 0x100
	v_mov_b32_e32 v20, 0
	s_sext_i32_i8 s4, s4
	s_cselect_b64 s[20:21], -1, 0
	s_add_i32 s84, s5, 0xe000
	v_add_u32_e32 v134, 0, v0
	v_add_u32_e32 v135, 0, v3
	v_mov_b32_e32 v136, 0x7f7f7f7f
	v_mov_b32_e32 v21, v20
	v_mov_b32_e32 v22, v20
	v_mov_b32_e32 v23, v20
	v_mov_b32_e32 v36, v20
	v_mov_b32_e32 v37, v20
	v_mov_b32_e32 v38, v20
	v_mov_b32_e32 v39, v20
	v_mov_b32_e32 v40, v20
	v_mov_b32_e32 v41, v20
	v_mov_b32_e32 v42, v20
	v_mov_b32_e32 v43, v20
	s_waitcnt vmcnt(4)
	v_pk_mov_b32 v[44:45], v[20:21], v[20:21]
	v_pk_mov_b32 v[46:47], v[20:21], v[20:21]
	v_pk_mov_b32 v[0:1], v[20:21], v[20:21]
	v_pk_mov_b32 v[2:3], v[20:21], v[20:21]
	v_pk_mov_b32 v[4:5], v[20:21], v[20:21]
	v_pk_mov_b32 v[6:7], v[20:21], v[20:21]
	v_pk_mov_b32 v[8:9], v[20:21], v[20:21]
	v_pk_mov_b32 v[10:11], v[20:21], v[20:21]
	v_pk_mov_b32 v[12:13], v[20:21], v[20:21]
	v_pk_mov_b32 v[14:15], v[20:21], v[20:21]
	v_pk_mov_b32 v[48:49], v[20:21], v[20:21]
	v_pk_mov_b32 v[50:51], v[20:21], v[20:21]
	v_pk_mov_b32 v[52:53], v[20:21], v[20:21]
	v_pk_mov_b32 v[54:55], v[20:21], v[20:21]
	v_pk_mov_b32 v[56:57], v[20:21], v[20:21]
	v_pk_mov_b32 v[58:59], v[20:21], v[20:21]
	v_pk_mov_b32 v[60:61], v[20:21], v[20:21]
	v_pk_mov_b32 v[62:63], v[20:21], v[20:21]
	v_pk_mov_b32 v[64:65], v[20:21], v[20:21]
	v_pk_mov_b32 v[66:67], v[20:21], v[20:21]
	v_pk_mov_b32 v[68:69], v[20:21], v[20:21]
	v_pk_mov_b32 v[70:71], v[20:21], v[20:21]
	v_pk_mov_b32 v[72:73], v[20:21], v[20:21]
	v_pk_mov_b32 v[74:75], v[20:21], v[20:21]
	v_pk_mov_b32 v[76:77], v[20:21], v[20:21]
	v_pk_mov_b32 v[78:79], v[20:21], v[20:21]
	v_pk_mov_b32 v[96:97], v[20:21], v[20:21]
	v_pk_mov_b32 v[98:99], v[20:21], v[20:21]
	v_pk_mov_b32 v[100:101], v[20:21], v[20:21]
	v_pk_mov_b32 v[102:103], v[20:21], v[20:21]
	v_pk_mov_b32 v[104:105], v[20:21], v[20:21]
	v_pk_mov_b32 v[106:107], v[20:21], v[20:21]
	v_pk_mov_b32 v[108:109], v[20:21], v[20:21]
	v_pk_mov_b32 v[110:111], v[20:21], v[20:21]
	v_pk_mov_b32 v[80:81], v[20:21], v[20:21]
	v_pk_mov_b32 v[82:83], v[20:21], v[20:21]
	v_pk_mov_b32 v[84:85], v[20:21], v[20:21]
	v_pk_mov_b32 v[86:87], v[20:21], v[20:21]
	v_pk_mov_b32 v[88:89], v[20:21], v[20:21]
	v_pk_mov_b32 v[90:91], v[20:21], v[20:21]
	v_pk_mov_b32 v[92:93], v[20:21], v[20:21]
	v_pk_mov_b32 v[94:95], v[20:21], v[20:21]
	v_pk_mov_b32 v[112:113], v[20:21], v[20:21]
	v_pk_mov_b32 v[114:115], v[20:21], v[20:21]
	v_pk_mov_b32 v[116:117], v[20:21], v[20:21]
	v_pk_mov_b32 v[118:119], v[20:21], v[20:21]
	v_pk_mov_b32 v[120:121], v[20:21], v[20:21]
	v_pk_mov_b32 v[122:123], v[20:21], v[20:21]
	v_pk_mov_b32 v[124:125], v[20:21], v[20:21]
	v_pk_mov_b32 v[126:127], v[20:21], v[20:21]
	v_pk_mov_b32 v[16:17], v[20:21], v[20:21]
	v_pk_mov_b32 v[18:19], v[20:21], v[20:21]
	v_pk_mov_b32 v[24:25], v[20:21], v[20:21]
	v_pk_mov_b32 v[26:27], v[20:21], v[20:21]
	v_pk_mov_b32 v[28:29], v[20:21], v[20:21]
	v_pk_mov_b32 v[30:31], v[20:21], v[20:21]
	v_pk_mov_b32 v[32:33], v[20:21], v[20:21]
	v_pk_mov_b32 v[34:35], v[20:21], v[20:21]
	s_barrier
	s_branch .LBB0_686
.LBB0_684:
	v_mov_b32_e32 v20, 0
	s_mov_b32 s4, s22
	s_mov_b32 s12, s24
	s_mov_b64 s[6:7], s[26:27]
	s_mov_b64 s[14:15], s[28:29]
	s_mov_b64 s[16:17], s[30:31]
	s_mov_b32 s42, s85
	v_mov_b32_e32 v21, v20
	v_pk_mov_b32 v[22:23], v[20:21], v[20:21]
	v_pk_mov_b32 v[36:37], v[20:21], v[20:21]
	v_pk_mov_b32 v[38:39], v[20:21], v[20:21]
	v_pk_mov_b32 v[40:41], v[20:21], v[20:21]
	v_pk_mov_b32 v[42:43], v[20:21], v[20:21]
	v_pk_mov_b32 v[44:45], v[20:21], v[20:21]
	v_pk_mov_b32 v[46:47], v[20:21], v[20:21]
	v_pk_mov_b32 v[0:1], v[20:21], v[20:21]
	v_pk_mov_b32 v[2:3], v[20:21], v[20:21]
	v_pk_mov_b32 v[4:5], v[20:21], v[20:21]
	v_pk_mov_b32 v[6:7], v[20:21], v[20:21]
	v_pk_mov_b32 v[8:9], v[20:21], v[20:21]
	v_pk_mov_b32 v[10:11], v[20:21], v[20:21]
	v_pk_mov_b32 v[12:13], v[20:21], v[20:21]
	v_pk_mov_b32 v[14:15], v[20:21], v[20:21]
	v_pk_mov_b32 v[48:49], v[20:21], v[20:21]
	v_pk_mov_b32 v[50:51], v[20:21], v[20:21]
	v_pk_mov_b32 v[52:53], v[20:21], v[20:21]
	v_pk_mov_b32 v[54:55], v[20:21], v[20:21]
	v_pk_mov_b32 v[56:57], v[20:21], v[20:21]
	v_pk_mov_b32 v[58:59], v[20:21], v[20:21]
	v_pk_mov_b32 v[60:61], v[20:21], v[20:21]
	v_pk_mov_b32 v[62:63], v[20:21], v[20:21]
	v_pk_mov_b32 v[64:65], v[20:21], v[20:21]
	v_pk_mov_b32 v[66:67], v[20:21], v[20:21]
	v_pk_mov_b32 v[68:69], v[20:21], v[20:21]
	v_pk_mov_b32 v[70:71], v[20:21], v[20:21]
	v_pk_mov_b32 v[72:73], v[20:21], v[20:21]
	v_pk_mov_b32 v[74:75], v[20:21], v[20:21]
	v_pk_mov_b32 v[76:77], v[20:21], v[20:21]
	v_pk_mov_b32 v[78:79], v[20:21], v[20:21]
	v_pk_mov_b32 v[96:97], v[20:21], v[20:21]
	v_pk_mov_b32 v[98:99], v[20:21], v[20:21]
	v_pk_mov_b32 v[100:101], v[20:21], v[20:21]
	v_pk_mov_b32 v[102:103], v[20:21], v[20:21]
	v_pk_mov_b32 v[104:105], v[20:21], v[20:21]
	v_pk_mov_b32 v[106:107], v[20:21], v[20:21]
	v_pk_mov_b32 v[108:109], v[20:21], v[20:21]
	v_pk_mov_b32 v[110:111], v[20:21], v[20:21]
	v_pk_mov_b32 v[80:81], v[20:21], v[20:21]
	v_pk_mov_b32 v[82:83], v[20:21], v[20:21]
	v_pk_mov_b32 v[84:85], v[20:21], v[20:21]
	v_pk_mov_b32 v[86:87], v[20:21], v[20:21]
	v_pk_mov_b32 v[88:89], v[20:21], v[20:21]
	v_pk_mov_b32 v[90:91], v[20:21], v[20:21]
	v_pk_mov_b32 v[92:93], v[20:21], v[20:21]
	v_pk_mov_b32 v[94:95], v[20:21], v[20:21]
	v_pk_mov_b32 v[112:113], v[20:21], v[20:21]
	v_pk_mov_b32 v[114:115], v[20:21], v[20:21]
	v_pk_mov_b32 v[116:117], v[20:21], v[20:21]
	v_pk_mov_b32 v[118:119], v[20:21], v[20:21]
	v_pk_mov_b32 v[120:121], v[20:21], v[20:21]
	v_pk_mov_b32 v[122:123], v[20:21], v[20:21]
	v_pk_mov_b32 v[124:125], v[20:21], v[20:21]
	v_pk_mov_b32 v[126:127], v[20:21], v[20:21]
	v_pk_mov_b32 v[16:17], v[20:21], v[20:21]
	v_pk_mov_b32 v[18:19], v[20:21], v[20:21]
	v_pk_mov_b32 v[24:25], v[20:21], v[20:21]
	v_pk_mov_b32 v[26:27], v[20:21], v[20:21]
	v_pk_mov_b32 v[28:29], v[20:21], v[20:21]
	v_pk_mov_b32 v[30:31], v[20:21], v[20:21]
	v_pk_mov_b32 v[32:33], v[20:21], v[20:21]
	v_pk_mov_b32 v[34:35], v[20:21], v[20:21]

.LBB0_1035:
	v_mbcnt_lo_u32_b32 v4, -1, 0
	v_mbcnt_hi_u32_b32 v4, -1, v4
	s_add_u32 s19, s50, 0x100
	v_add_u32_e32 v4, s0, v4
	v_lshl_add_u32 v4, v4, 4, 0
	v_add_u32_e32 v4, 0x21000, v4
	s_addc_u32 s25, s51, 0
	ds_write_b128 v4, v[0:3]
	s_add_u32 s81, s56, 0x100
	v_mov_b32_e32 v0, 0
	s_addc_u32 s82, s57, 0
	s_mov_b32 s83, -2
	v_mov_b32_e32 v1, v0
	v_pk_mov_b32 v[2:3], v[0:1], v[0:1]
	v_pk_mov_b32 v[8:9], v[0:1], v[0:1]
	v_pk_mov_b32 v[10:11], v[0:1], v[0:1]
	v_pk_mov_b32 v[16:17], v[0:1], v[0:1]
	v_pk_mov_b32 v[18:19], v[0:1], v[0:1]
	v_pk_mov_b32 v[24:25], v[0:1], v[0:1]
	v_pk_mov_b32 v[26:27], v[0:1], v[0:1]
	v_pk_mov_b32 v[32:33], v[0:1], v[0:1]
	v_pk_mov_b32 v[34:35], v[0:1], v[0:1]
	v_pk_mov_b32 v[44:45], v[0:1], v[0:1]
	v_pk_mov_b32 v[46:47], v[0:1], v[0:1]
	v_pk_mov_b32 v[52:53], v[0:1], v[0:1]
	v_pk_mov_b32 v[54:55], v[0:1], v[0:1]
	v_pk_mov_b32 v[60:61], v[0:1], v[0:1]
	v_pk_mov_b32 v[62:63], v[0:1], v[0:1]
	v_pk_mov_b32 v[4:5], v[0:1], v[0:1]
	v_pk_mov_b32 v[6:7], v[0:1], v[0:1]
	v_pk_mov_b32 v[12:13], v[0:1], v[0:1]
	v_pk_mov_b32 v[14:15], v[0:1], v[0:1]
	v_pk_mov_b32 v[20:21], v[0:1], v[0:1]
	v_pk_mov_b32 v[22:23], v[0:1], v[0:1]
	v_pk_mov_b32 v[28:29], v[0:1], v[0:1]
	v_pk_mov_b32 v[30:31], v[0:1], v[0:1]
	v_pk_mov_b32 v[40:41], v[0:1], v[0:1]
	v_pk_mov_b32 v[42:43], v[0:1], v[0:1]
	v_pk_mov_b32 v[48:49], v[0:1], v[0:1]
	v_pk_mov_b32 v[50:51], v[0:1], v[0:1]
	v_pk_mov_b32 v[56:57], v[0:1], v[0:1]
	v_pk_mov_b32 v[58:59], v[0:1], v[0:1]
	v_pk_mov_b32 v[64:65], v[0:1], v[0:1]
	v_pk_mov_b32 v[66:67], v[0:1], v[0:1]
	v_pk_mov_b32 v[68:69], v[0:1], v[0:1]
	v_pk_mov_b32 v[70:71], v[0:1], v[0:1]
	v_pk_mov_b32 v[76:77], v[0:1], v[0:1]
	v_pk_mov_b32 v[78:79], v[0:1], v[0:1]
	v_pk_mov_b32 v[84:85], v[0:1], v[0:1]
	v_pk_mov_b32 v[86:87], v[0:1], v[0:1]
	v_pk_mov_b32 v[92:93], v[0:1], v[0:1]
	v_pk_mov_b32 v[94:95], v[0:1], v[0:1]
	v_pk_mov_b32 v[100:101], v[0:1], v[0:1]
	v_pk_mov_b32 v[102:103], v[0:1], v[0:1]
	v_pk_mov_b32 v[112:113], v[0:1], v[0:1]
	v_pk_mov_b32 v[114:115], v[0:1], v[0:1]
	v_pk_mov_b32 v[128:129], v[0:1], v[0:1]
	v_pk_mov_b32 v[130:131], v[0:1], v[0:1]
	v_pk_mov_b32 v[136:137], v[0:1], v[0:1]
	v_pk_mov_b32 v[138:139], v[0:1], v[0:1]
	v_pk_mov_b32 v[72:73], v[0:1], v[0:1]
	v_pk_mov_b32 v[74:75], v[0:1], v[0:1]
	v_pk_mov_b32 v[80:81], v[0:1], v[0:1]
	v_pk_mov_b32 v[82:83], v[0:1], v[0:1]
	v_pk_mov_b32 v[88:89], v[0:1], v[0:1]
	v_pk_mov_b32 v[90:91], v[0:1], v[0:1]
	v_pk_mov_b32 v[96:97], v[0:1], v[0:1]
	v_pk_mov_b32 v[98:99], v[0:1], v[0:1]
	v_pk_mov_b32 v[108:109], v[0:1], v[0:1]
	v_pk_mov_b32 v[110:111], v[0:1], v[0:1]
	v_pk_mov_b32 v[124:125], v[0:1], v[0:1]
	v_pk_mov_b32 v[126:127], v[0:1], v[0:1]
	v_pk_mov_b32 v[132:133], v[0:1], v[0:1]
	v_pk_mov_b32 v[134:135], v[0:1], v[0:1]
	v_pk_mov_b32 v[140:141], v[0:1], v[0:1]
	v_pk_mov_b32 v[142:143], v[0:1], v[0:1]
	s_branch .LBB0_1037

.LBB0_1152:
	s_and_b64 s[50:51], s[26:27], exec
	s_cselect_b32 s5, s21, s35
	s_cselect_b32 s29, s20, s34
	s_cselect_b32 s72, s23, s37
	s_cselect_b32 s73, s22, s36
	s_cselect_b32 s74, s25, s47
	s_cselect_b32 s75, s24, s46
	s_add_u32 s76, s36, 0x100
	s_addc_u32 s77, s37, 0
	s_add_u32 s78, s46, 0x100
	v_mov_b32_e32 v20, 0
	s_addc_u32 s79, s47, 0
	s_mov_b32 s80, -2
	v_mov_b32_e32 v21, v20
	v_pk_mov_b32 v[22:23], v[20:21], v[20:21]
	v_pk_mov_b32 v[28:29], v[20:21], v[20:21]
	v_pk_mov_b32 v[30:31], v[20:21], v[20:21]
	v_pk_mov_b32 v[48:49], v[20:21], v[20:21]
	v_pk_mov_b32 v[50:51], v[20:21], v[20:21]
	v_pk_mov_b32 v[52:53], v[20:21], v[20:21]
	v_pk_mov_b32 v[54:55], v[20:21], v[20:21]
	v_pk_mov_b32 v[0:1], v[20:21], v[20:21]
	v_pk_mov_b32 v[2:3], v[20:21], v[20:21]
	v_pk_mov_b32 v[4:5], v[20:21], v[20:21]
	v_pk_mov_b32 v[6:7], v[20:21], v[20:21]
	v_pk_mov_b32 v[12:13], v[20:21], v[20:21]
	v_pk_mov_b32 v[14:15], v[20:21], v[20:21]
	v_pk_mov_b32 v[24:25], v[20:21], v[20:21]
	v_pk_mov_b32 v[26:27], v[20:21], v[20:21]
	v_pk_mov_b32 v[40:41], v[20:21], v[20:21]
	v_pk_mov_b32 v[42:43], v[20:21], v[20:21]
	s_waitcnt vmcnt(4)
	v_pk_mov_b32 v[44:45], v[20:21], v[20:21]
	v_pk_mov_b32 v[46:47], v[20:21], v[20:21]
	v_pk_mov_b32 v[56:57], v[20:21], v[20:21]
	v_pk_mov_b32 v[58:59], v[20:21], v[20:21]
	v_pk_mov_b32 v[60:61], v[20:21], v[20:21]
	v_pk_mov_b32 v[62:63], v[20:21], v[20:21]
	v_pk_mov_b32 v[64:65], v[20:21], v[20:21]
	v_pk_mov_b32 v[66:67], v[20:21], v[20:21]
	v_pk_mov_b32 v[68:69], v[20:21], v[20:21]
	v_pk_mov_b32 v[70:71], v[20:21], v[20:21]
	v_pk_mov_b32 v[80:81], v[20:21], v[20:21]
	v_pk_mov_b32 v[82:83], v[20:21], v[20:21]
	v_pk_mov_b32 v[84:85], v[20:21], v[20:21]
	v_pk_mov_b32 v[86:87], v[20:21], v[20:21]
	v_pk_mov_b32 v[96:97], v[20:21], v[20:21]
	v_pk_mov_b32 v[98:99], v[20:21], v[20:21]
	v_pk_mov_b32 v[100:101], v[20:21], v[20:21]
	v_pk_mov_b32 v[102:103], v[20:21], v[20:21]
	v_pk_mov_b32 v[112:113], v[20:21], v[20:21]
	v_pk_mov_b32 v[114:115], v[20:21], v[20:21]
	v_pk_mov_b32 v[116:117], v[20:21], v[20:21]
	v_pk_mov_b32 v[118:119], v[20:21], v[20:21]
	v_pk_mov_b32 v[72:73], v[20:21], v[20:21]
	v_pk_mov_b32 v[74:75], v[20:21], v[20:21]
	v_pk_mov_b32 v[76:77], v[20:21], v[20:21]
	v_pk_mov_b32 v[78:79], v[20:21], v[20:21]
	v_pk_mov_b32 v[88:89], v[20:21], v[20:21]
	v_pk_mov_b32 v[90:91], v[20:21], v[20:21]
	v_pk_mov_b32 v[92:93], v[20:21], v[20:21]
	v_pk_mov_b32 v[94:95], v[20:21], v[20:21]
	v_pk_mov_b32 v[104:105], v[20:21], v[20:21]
	v_pk_mov_b32 v[106:107], v[20:21], v[20:21]
	v_pk_mov_b32 v[108:109], v[20:21], v[20:21]
	v_pk_mov_b32 v[110:111], v[20:21], v[20:21]
	v_pk_mov_b32 v[120:121], v[20:21], v[20:21]
	v_pk_mov_b32 v[122:123], v[20:21], v[20:21]
	v_pk_mov_b32 v[124:125], v[20:21], v[20:21]
	v_pk_mov_b32 v[126:127], v[20:21], v[20:21]
	v_pk_mov_b32 v[36:37], v[20:21], v[20:21]
	v_pk_mov_b32 v[38:39], v[20:21], v[20:21]
	v_pk_mov_b32 v[32:33], v[20:21], v[20:21]
	v_pk_mov_b32 v[34:35], v[20:21], v[20:21]
	v_pk_mov_b32 v[16:17], v[20:21], v[20:21]
	v_pk_mov_b32 v[18:19], v[20:21], v[20:21]
	v_pk_mov_b32 v[8:9], v[20:21], v[20:21]
	v_pk_mov_b32 v[10:11], v[20:21], v[20:21]

.LBB0_1329:
	v_readlane_b32 s17, v255, 0
	s_bfe_u32 s5, s17, 0x20006
	s_lshl_b32 s38, s3, 6
	v_and_b32_e32 v2, 48, v0
	v_lshlrev_b32_e32 v4, 6, v0
	s_movk_i32 s14, 0x3c0
	v_and_or_b32 v2, v4, s14, v2
	s_add_u32 s14, s8, 0x80
	s_waitcnt vmcnt(2)
	s_barrier
	s_addc_u32 s15, s9, 0
	s_add_i32 s56, s47, 0x18000
	s_mov_b32 s16, m0
	s_mov_b32 m0, s56
	s_nop 2
	global_load_lds_dwordx4 v130, s[14:15]
	s_mov_b32 m0, s16
	s_add_i32 s57, s47, 0x1a000
	s_mov_b32 s16, m0
	s_mov_b32 m0, s57
	s_nop 2
	global_load_lds_dwordx4 v131, s[14:15]
	s_mov_b32 m0, s16
	s_add_u32 s14, s0, 0x80
	s_addc_u32 s15, s1, 0
	s_add_i32 s58, s47, 0x8000
	s_mov_b32 s16, m0
	s_mov_b32 m0, s58
	s_nop 2
	global_load_lds_dwordx4 v132, s[14:15]
	s_mov_b32 m0, s16
	s_add_i32 s59, s47, 0xa000
	s_mov_b32 s16, m0
	s_mov_b32 m0, s59
	s_nop 2
	global_load_lds_dwordx4 v133, s[14:15]
	s_mov_b32 m0, s16
	s_add_u32 s14, s8, 0x40080
	s_addc_u32 s15, s9, 0
	s_add_i32 s60, s47, 0x1c000
	s_mov_b32 s16, m0
	s_mov_b32 m0, s60
	s_nop 2
	global_load_lds_dwordx4 v130, s[14:15]
	s_mov_b32 m0, s16
	v_and_b32_e32 v1, 0xfffffc00, v1
	v_lshlrev_b32_e32 v0, 2, v0
	s_add_i32 s61, s47, 0x1e000
	s_mov_b32 s16, m0
	s_mov_b32 m0, s61
	s_nop 2
	global_load_lds_dwordx4 v131, s[14:15]
	s_mov_b32 m0, s16
	v_lshl_add_u32 v3, s3, 13, v1
	v_and_b32_e32 v0, 32, v0
	v_lshl_add_u32 v1, s5, 12, v1
	s_waitcnt vmcnt(6)
	s_add_i32 s62, s47, 0xc000
	v_bitop3_b32 v3, v2, v3, v0 bitop3:0xde
	v_bitop3_b32 v0, v2, v1, v0 bitop3:0xde
	s_cmpk_lt_u32 s17, 0x100
	v_mov_b32_e32 v20, 0
	s_sext_i32_i8 s6, s6
	s_cselect_b64 s[14:15], -1, 0
	s_add_i32 s63, s47, 0xe000
	v_add_u32_e32 v134, 0, v0
	v_add_u32_e32 v135, 0, v3
	v_mov_b32_e32 v136, 0x7f7f7f7f
	v_mov_b64_e32 v[128:129], 0xff
	v_mov_b32_e32 v21, v20
	v_pk_mov_b32 v[22:23], v[20:21], v[20:21]
	v_pk_mov_b32 v[36:37], v[20:21], v[20:21]
	v_pk_mov_b32 v[38:39], v[20:21], v[20:21]
	v_pk_mov_b32 v[48:49], v[20:21], v[20:21]
	v_pk_mov_b32 v[50:51], v[20:21], v[20:21]
	v_pk_mov_b32 v[52:53], v[20:21], v[20:21]
	v_pk_mov_b32 v[54:55], v[20:21], v[20:21]
	v_pk_mov_b32 v[0:1], v[20:21], v[20:21]
	v_pk_mov_b32 v[2:3], v[20:21], v[20:21]
	v_pk_mov_b32 v[4:5], v[20:21], v[20:21]
	v_pk_mov_b32 v[6:7], v[20:21], v[20:21]
	v_pk_mov_b32 v[16:17], v[20:21], v[20:21]
	v_pk_mov_b32 v[18:19], v[20:21], v[20:21]
	v_pk_mov_b32 v[24:25], v[20:21], v[20:21]
	v_pk_mov_b32 v[26:27], v[20:21], v[20:21]
	v_pk_mov_b32 v[40:41], v[20:21], v[20:21]
	v_pk_mov_b32 v[42:43], v[20:21], v[20:21]
	s_waitcnt vmcnt(4)
	v_pk_mov_b32 v[44:45], v[20:21], v[20:21]
	v_pk_mov_b32 v[46:47], v[20:21], v[20:21]
	v_pk_mov_b32 v[56:57], v[20:21], v[20:21]
	v_pk_mov_b32 v[58:59], v[20:21], v[20:21]
	v_pk_mov_b32 v[60:61], v[20:21], v[20:21]
	v_pk_mov_b32 v[62:63], v[20:21], v[20:21]
	v_pk_mov_b32 v[68:69], v[20:21], v[20:21]
	v_pk_mov_b32 v[70:71], v[20:21], v[20:21]
	v_pk_mov_b32 v[76:77], v[20:21], v[20:21]
	v_pk_mov_b32 v[78:79], v[20:21], v[20:21]
	v_pk_mov_b32 v[104:105], v[20:21], v[20:21]
	v_pk_mov_b32 v[106:107], v[20:21], v[20:21]
	v_pk_mov_b32 v[116:117], v[20:21], v[20:21]
	v_pk_mov_b32 v[118:119], v[20:21], v[20:21]
	v_pk_mov_b32 v[112:113], v[20:21], v[20:21]
	v_pk_mov_b32 v[114:115], v[20:21], v[20:21]
	v_pk_mov_b32 v[108:109], v[20:21], v[20:21]
	v_pk_mov_b32 v[110:111], v[20:21], v[20:21]
	v_pk_mov_b32 v[84:85], v[20:21], v[20:21]
	v_pk_mov_b32 v[86:87], v[20:21], v[20:21]
	v_pk_mov_b32 v[80:81], v[20:21], v[20:21]
	v_pk_mov_b32 v[82:83], v[20:21], v[20:21]
	v_pk_mov_b32 v[92:93], v[20:21], v[20:21]
	v_pk_mov_b32 v[94:95], v[20:21], v[20:21]
	v_pk_mov_b32 v[100:101], v[20:21], v[20:21]
	v_pk_mov_b32 v[102:103], v[20:21], v[20:21]
	v_pk_mov_b32 v[124:125], v[20:21], v[20:21]
	v_pk_mov_b32 v[126:127], v[20:21], v[20:21]
	v_pk_mov_b32 v[120:121], v[20:21], v[20:21]
	v_pk_mov_b32 v[122:123], v[20:21], v[20:21]
	v_pk_mov_b32 v[96:97], v[20:21], v[20:21]
	v_pk_mov_b32 v[98:99], v[20:21], v[20:21]
	v_pk_mov_b32 v[88:89], v[20:21], v[20:21]
	v_pk_mov_b32 v[90:91], v[20:21], v[20:21]
	v_pk_mov_b32 v[72:73], v[20:21], v[20:21]
	v_pk_mov_b32 v[74:75], v[20:21], v[20:21]
	v_pk_mov_b32 v[64:65], v[20:21], v[20:21]
	v_pk_mov_b32 v[66:67], v[20:21], v[20:21]
	v_pk_mov_b32 v[32:33], v[20:21], v[20:21]
	v_pk_mov_b32 v[34:35], v[20:21], v[20:21]
	v_pk_mov_b32 v[28:29], v[20:21], v[20:21]
	v_pk_mov_b32 v[30:31], v[20:21], v[20:21]
	v_pk_mov_b32 v[12:13], v[20:21], v[20:21]
	v_pk_mov_b32 v[14:15], v[20:21], v[20:21]
	v_pk_mov_b32 v[8:9], v[20:21], v[20:21]
	v_pk_mov_b32 v[10:11], v[20:21], v[20:21]
	s_barrier
	s_branch .LBB0_1332
.LBB0_1330:
	v_mov_b32_e32 v20, 0
	s_mov_b32 s6, s16
	s_mov_b32 s4, s18
	s_mov_b64 s[0:1], s[20:21]
	s_mov_b64 s[8:9], s[22:23]
	s_mov_b64 s[10:11], s[24:25]
	s_mov_b32 s48, s64
	v_mov_b32_e32 v21, v20
	v_pk_mov_b32 v[22:23], v[20:21], v[20:21]
	v_pk_mov_b32 v[36:37], v[20:21], v[20:21]
	v_pk_mov_b32 v[38:39], v[20:21], v[20:21]
	v_pk_mov_b32 v[48:49], v[20:21], v[20:21]
	v_pk_mov_b32 v[50:51], v[20:21], v[20:21]
	v_pk_mov_b32 v[52:53], v[20:21], v[20:21]
	v_pk_mov_b32 v[54:55], v[20:21], v[20:21]
	v_pk_mov_b32 v[0:1], v[20:21], v[20:21]
	v_pk_mov_b32 v[2:3], v[20:21], v[20:21]
	v_pk_mov_b32 v[4:5], v[20:21], v[20:21]
	v_pk_mov_b32 v[6:7], v[20:21], v[20:21]
	v_pk_mov_b32 v[16:17], v[20:21], v[20:21]
	v_pk_mov_b32 v[18:19], v[20:21], v[20:21]
	v_pk_mov_b32 v[24:25], v[20:21], v[20:21]
	v_pk_mov_b32 v[26:27], v[20:21], v[20:21]
	v_pk_mov_b32 v[40:41], v[20:21], v[20:21]
	v_pk_mov_b32 v[42:43], v[20:21], v[20:21]
	v_pk_mov_b32 v[44:45], v[20:21], v[20:21]
	v_pk_mov_b32 v[46:47], v[20:21], v[20:21]
	v_pk_mov_b32 v[56:57], v[20:21], v[20:21]
	v_pk_mov_b32 v[58:59], v[20:21], v[20:21]
	v_pk_mov_b32 v[60:61], v[20:21], v[20:21]
	v_pk_mov_b32 v[62:63], v[20:21], v[20:21]
	v_pk_mov_b32 v[68:69], v[20:21], v[20:21]
	v_pk_mov_b32 v[70:71], v[20:21], v[20:21]
	v_pk_mov_b32 v[76:77], v[20:21], v[20:21]
	v_pk_mov_b32 v[78:79], v[20:21], v[20:21]
	v_pk_mov_b32 v[104:105], v[20:21], v[20:21]
	v_pk_mov_b32 v[106:107], v[20:21], v[20:21]
	v_pk_mov_b32 v[116:117], v[20:21], v[20:21]
	v_pk_mov_b32 v[118:119], v[20:21], v[20:21]
	v_pk_mov_b32 v[112:113], v[20:21], v[20:21]
	v_pk_mov_b32 v[114:115], v[20:21], v[20:21]
	v_pk_mov_b32 v[108:109], v[20:21], v[20:21]
	v_pk_mov_b32 v[110:111], v[20:21], v[20:21]
	v_pk_mov_b32 v[84:85], v[20:21], v[20:21]
	v_pk_mov_b32 v[86:87], v[20:21], v[20:21]
	v_pk_mov_b32 v[80:81], v[20:21], v[20:21]
	v_pk_mov_b32 v[82:83], v[20:21], v[20:21]
	v_pk_mov_b32 v[92:93], v[20:21], v[20:21]
	v_pk_mov_b32 v[94:95], v[20:21], v[20:21]
	v_pk_mov_b32 v[100:101], v[20:21], v[20:21]
	v_pk_mov_b32 v[102:103], v[20:21], v[20:21]
	v_pk_mov_b32 v[124:125], v[20:21], v[20:21]
	v_pk_mov_b32 v[126:127], v[20:21], v[20:21]
	v_pk_mov_b32 v[120:121], v[20:21], v[20:21]
	v_pk_mov_b32 v[122:123], v[20:21], v[20:21]
	v_pk_mov_b32 v[96:97], v[20:21], v[20:21]
	v_pk_mov_b32 v[98:99], v[20:21], v[20:21]
	v_pk_mov_b32 v[88:89], v[20:21], v[20:21]
	v_pk_mov_b32 v[90:91], v[20:21], v[20:21]
	v_pk_mov_b32 v[72:73], v[20:21], v[20:21]
	v_pk_mov_b32 v[74:75], v[20:21], v[20:21]
	v_pk_mov_b32 v[64:65], v[20:21], v[20:21]
	v_pk_mov_b32 v[66:67], v[20:21], v[20:21]
	v_pk_mov_b32 v[32:33], v[20:21], v[20:21]
	v_pk_mov_b32 v[34:35], v[20:21], v[20:21]
	v_pk_mov_b32 v[28:29], v[20:21], v[20:21]
	v_pk_mov_b32 v[30:31], v[20:21], v[20:21]
	v_pk_mov_b32 v[12:13], v[20:21], v[20:21]
	v_pk_mov_b32 v[14:15], v[20:21], v[20:21]
	v_pk_mov_b32 v[8:9], v[20:21], v[20:21]
	v_pk_mov_b32 v[10:11], v[20:21], v[20:21]
